# EpiRes epilogue: 14 of 16 x-chunk loads issued up front, row-sum shuffles batched into 2 LDS round trips (same fused math/order)
# baseline (speedup 1.0000x reference)
; __device__ __forceinline__ unsigned cvt_pk_bf16(float lo, float hi) { const f32x2_t v = {lo, hi}; const bf16x2_t b = __builtin_convertvector(v, bf16x2_t); return __builtin_bit_cast(unsigned, b); }
; #define EPIRES_LOAD(buf, g) do { _Pragma("unroll") for (int bj = 0; bj < 2; ++bj) xb[buf][bj] = *(const u32x4*)(x + EPIRES_OFF(g, bj)); } while (0)
;     __device__ __forceinline__ void operator()(const f32x4 (&acc)[2][2][4][2], const Unit& u, int wr, int wc, int fr, int fq, int ui) const {
;         const int col0 = u.pn * BM + wc * 32 + 8 * fq;
;         const size_t off0 = ((size_t)(u.pm * (D / 64) + (col0 >> 6)) * 256 + wr * 64 + fr) * 64 + (col0 & 63);
;         f32x4 cr[2][2];
; #pragma unroll
;         for (int bj = 0; bj < 2; ++bj)
; #pragma unroll
;             for (int n = 0; n < 2; ++n) cr[bj][n] = *(const f32x4*)(cres + col0 + bj * HALF + n * 4);
;         u32x4 xb[3][2];
;     ...
;         EPIRES_LOAD(0, 0); EPIRES_LOAD(1, 1); EPIRES_LOAD(2, 2);
; #pragma unroll
;         for (int g = 0; g < 8; ++g) {
;             const int ai = g >> 2, m = g & 3;
;             const int row_ = u.pm * BM + ai * HALF + wr * 64 + m * 16 + fr;
;             float sq = 0.f;
; #pragma unroll
;             for (int bj = 0; bj < 2; ++bj) {
;                 u32x4 xs;
; #pragma unroll
;                 for (int n = 0; n < 2; ++n) {
;                     const unsigned p0 = xb[g % 3][bj][2 * n], p1 = xb[g % 3][bj][2 * n + 1];
;                     const f32x4 xo = {__builtin_bit_cast(float, p0 << 16), __builtin_bit_cast(float, p0 & 0xFFFF0000u), __builtin_bit_cast(float, p1 << 16), __builtin_bit_cast(float, p1 & 0xFFFF0000u)};
;                     const f32x4 xn = xo + cr[bj][n] * acc[ai][bj][m][n];
;                     sq += (xn[0] * xn[0] + xn[1] * xn[1]) + (xn[2] * xn[2] + xn[3] * xn[3]);
;                     if (n == 0) { xs.x = cvt_pk_bf16(xn[0], xn[1]); xs.y = cvt_pk_bf16(xn[2], xn[3]); } else { xs.z = cvt_pk_bf16(xn[0], xn[1]); xs.w = cvt_pk_bf16(xn[2], xn[3]); }
;                 }
;                 *(u32x4*)(x + EPIRES_OFF(g, bj)) = xs;
;             }
;             sq += __shfl_xor(sq, 16); sq += __shfl_xor(sq, 32);
;             if (fq == 0) ss[(size_t)row_ * 32 + u.pn * 4 + wc] = sq;
;             if (g + 3 < 8) EPIRES_LOAD(g % 3, g + 3);
.LBB0_1399:
	s_lshl_b32 s18, s48, 8
	s_or_b32 s20, s18, s39
	s_lshl_b32 s18, s49, 5
	s_ashr_i32 s19, s20, 6
	s_add_i32 s18, s19, s18
	s_ashr_i32 s19, s18, 31
	v_or_b32_e32 v88, s20, v194
	v_bitop3_b32 v128, s20, 56, v194 bitop3:0xc8
	s_lshl_b64 s[18:19], s[18:19], 15
	v_ashrrev_i32_e32 v89, 31, v88
	v_lshl_add_u64 v[146:147], v[186:187], 0, s[18:19]
	v_lshlrev_b32_e32 v128, 1, v128
	v_lshl_add_u64 v[92:93], v[88:89], 2, s[10:11]
	v_lshl_add_u64 v[188:189], v[146:147], 0, v[128:129]
	global_load_dwordx4 v[100:103], v[92:93], off offset:16
	global_load_dwordx4 v[108:111], v[92:93], off
	global_load_dwordx4 v[88:91], v[92:93], off offset:528
	s_nop 0
	global_load_dwordx4 v[92:95], v[92:93], off offset:512
	s_mov_b64 s[20:21], 0x1000
	v_lshl_add_u64 v[172:173], v[188:189], 0, s[20:21]
	s_mov_b64 s[20:21], 0x5000
	v_lshl_add_u64 v[174:175], v[188:189], 0, s[20:21]
	s_mov_b64 s[20:21], 0x11000
	v_lshl_add_u64 v[190:191], v[188:189], 0, s[20:21]
	s_mov_b64 s[20:21], 0x15000
	v_lshl_add_u64 v[192:193], v[188:189], 0, s[20:21]
	global_load_dwordx4 v[146:149], v[172:173], off offset:-4096
	global_load_dwordx4 v[150:153], v[190:191], off offset:-4096
	global_load_dwordx4 v[154:157], v[172:173], off offset:-2048
	global_load_dwordx4 v[158:161], v[190:191], off offset:-2048
	global_load_dwordx4 v[162:165], v[172:173], off
	global_load_dwordx4 v[166:169], v[190:191], off
	global_load_dwordx4 v[196:199], v[172:173], off offset:2048
	global_load_dwordx4 v[200:203], v[190:191], off offset:2048
	global_load_dwordx4 v[204:207], v[174:175], off offset:-4096
	global_load_dwordx4 v[208:211], v[192:193], off offset:-4096
	global_load_dwordx4 v[212:215], v[174:175], off offset:-2048
	global_load_dwordx4 v[216:219], v[192:193], off offset:-2048
	global_load_dwordx4 v[220:223], v[174:175], off
	global_load_dwordx4 v[224:227], v[192:193], off
	s_waitcnt vmcnt(0)
	v_lshlrev_b32_e32 v128, 16, v146
	v_and_b32_e32 v146, 0xffff0000, v146
	v_fma_f32 v142, v142, v108, v128
	v_fma_f32 v143, v143, v109, v146
	v_lshlrev_b32_e32 v128, 16, v147
	v_and_b32_e32 v147, 0xffff0000, v147
	v_fma_f32 v144, v144, v110, v128
	v_fma_f32 v145, v145, v111, v147
	v_mul_f32_e32 v146, v143, v143
	v_mul_f32_e32 v147, v145, v145
	v_fmac_f32_e32 v146, v142, v142
	v_fmac_f32_e32 v147, v144, v144
	v_add_f32_e32 v146, v146, v147
	v_lshlrev_b32_e32 v128, 16, v148
	v_and_b32_e32 v148, 0xffff0000, v148
	v_fma_f32 v138, v138, v100, v128
	v_fma_f32 v139, v139, v101, v148
	v_lshlrev_b32_e32 v128, 16, v149
	v_and_b32_e32 v149, 0xffff0000, v149
	v_fma_f32 v140, v140, v102, v128
	v_fma_f32 v141, v141, v103, v149
	v_mul_f32_e32 v148, v139, v139
	v_mul_f32_e32 v149, v141, v141
	v_fmac_f32_e32 v148, v138, v138
	v_fmac_f32_e32 v149, v140, v140
	v_add_f32_e32 v148, v148, v149
	v_add_f32_e32 v128, v146, v148
	v_cvt_pk_bf16_f32 v146, v142, v143
	v_cvt_pk_bf16_f32 v147, v144, v145
	v_cvt_pk_bf16_f32 v148, v138, v139
	v_cvt_pk_bf16_f32 v149, v140, v141
	v_mov_b32_e32 v142, v128
	global_store_dwordx4 v[172:173], v[146:149], off offset:-4096
	v_lshlrev_b32_e32 v128, 16, v150
	v_and_b32_e32 v150, 0xffff0000, v150
	v_fma_f32 v134, v134, v92, v128
	v_fma_f32 v135, v135, v93, v150
	v_lshlrev_b32_e32 v128, 16, v151
	v_and_b32_e32 v151, 0xffff0000, v151
	v_fma_f32 v136, v136, v94, v128
	v_fma_f32 v137, v137, v95, v151
	v_mul_f32_e32 v150, v135, v135
	v_mul_f32_e32 v151, v137, v137
	v_fmac_f32_e32 v150, v134, v134
	v_fmac_f32_e32 v151, v136, v136
	v_add_f32_e32 v150, v150, v151
	v_lshlrev_b32_e32 v128, 16, v152
	v_and_b32_e32 v152, 0xffff0000, v152
	v_fma_f32 v130, v130, v88, v128
	v_fma_f32 v131, v131, v89, v152
	v_lshlrev_b32_e32 v128, 16, v153
	v_and_b32_e32 v153, 0xffff0000, v153
	v_fma_f32 v132, v132, v90, v128
	v_fma_f32 v133, v133, v91, v153
	v_mul_f32_e32 v152, v131, v131
	v_mul_f32_e32 v153, v133, v133
	v_fmac_f32_e32 v152, v130, v130
	v_fmac_f32_e32 v153, v132, v132
	v_add_f32_e32 v152, v152, v153
	v_add_f32_e32 v128, v142, v150
	v_add_f32_e32 v128, v128, v152
	v_cvt_pk_bf16_f32 v150, v134, v135
	v_cvt_pk_bf16_f32 v151, v136, v137
	v_cvt_pk_bf16_f32 v152, v130, v131
	v_cvt_pk_bf16_f32 v153, v132, v133
	v_mov_b32_e32 v142, v128
	global_store_dwordx4 v[190:191], v[150:153], off offset:-4096
	global_load_dwordx4 v[138:141], v[174:175], off offset:2048
	global_load_dwordx4 v[134:137], v[192:193], off offset:2048
	v_lshlrev_b32_e32 v128, 16, v154
	v_and_b32_e32 v154, 0xffff0000, v154
	v_fma_f32 v124, v124, v108, v128
	v_fma_f32 v125, v125, v109, v154
	v_lshlrev_b32_e32 v128, 16, v155
	v_and_b32_e32 v155, 0xffff0000, v155
	v_fma_f32 v126, v126, v110, v128
	v_fma_f32 v127, v127, v111, v155
	v_mul_f32_e32 v154, v125, v125
	v_mul_f32_e32 v155, v127, v127
	v_fmac_f32_e32 v154, v124, v124
	v_fmac_f32_e32 v155, v126, v126
	v_add_f32_e32 v154, v154, v155
	v_lshlrev_b32_e32 v128, 16, v156
	v_and_b32_e32 v156, 0xffff0000, v156
	v_fma_f32 v120, v120, v100, v128
	v_fma_f32 v121, v121, v101, v156
	v_lshlrev_b32_e32 v128, 16, v157
	v_and_b32_e32 v157, 0xffff0000, v157
	v_fma_f32 v122, v122, v102, v128
	v_fma_f32 v123, v123, v103, v157
	v_mul_f32_e32 v156, v121, v121
	v_mul_f32_e32 v157, v123, v123
	v_fmac_f32_e32 v156, v120, v120
	v_fmac_f32_e32 v157, v122, v122
	v_add_f32_e32 v156, v156, v157
	v_add_f32_e32 v128, v154, v156
	v_cvt_pk_bf16_f32 v154, v124, v125
	v_cvt_pk_bf16_f32 v155, v126, v127
	v_cvt_pk_bf16_f32 v156, v120, v121
	v_cvt_pk_bf16_f32 v157, v122, v123
	v_mov_b32_e32 v124, v128
	global_store_dwordx4 v[172:173], v[154:157], off offset:-2048
	v_lshlrev_b32_e32 v128, 16, v158
	v_and_b32_e32 v158, 0xffff0000, v158
	v_fma_f32 v116, v116, v92, v128
	v_fma_f32 v117, v117, v93, v158
	v_lshlrev_b32_e32 v128, 16, v159
; __device__ __forceinline__ unsigned cvt_pk_bf16(float lo, float hi) { const f32x2_t v = {lo, hi}; const bf16x2_t b = __builtin_convertvector(v, bf16x2_t); return __builtin_bit_cast(unsigned, b); }
;     __device__ __forceinline__ void operator()(const f32x4 (&acc)[2][2][4][2], const Unit& u, int wr, int wc, int fr, int fq, int ui) const {
;     ...
;             for (int bj = 0; bj < 2; ++bj) {
;                 u32x4 xs;
; #pragma unroll
;                 for (int n = 0; n < 2; ++n) {
;                     const unsigned p0 = xb[g % 3][bj][2 * n], p1 = xb[g % 3][bj][2 * n + 1];
;                     const f32x4 xo = {__builtin_bit_cast(float, p0 << 16), __builtin_bit_cast(float, p0 & 0xFFFF0000u), __builtin_bit_cast(float, p1 << 16), __builtin_bit_cast(float, p1 & 0xFFFF0000u)};
;                     const f32x4 xn = xo + cr[bj][n] * acc[ai][bj][m][n];
;                     sq += (xn[0] * xn[0] + xn[1] * xn[1]) + (xn[2] * xn[2] + xn[3] * xn[3]);
;                     if (n == 0) { xs.x = cvt_pk_bf16(xn[0], xn[1]); xs.y = cvt_pk_bf16(xn[2], xn[3]); } else { xs.z = cvt_pk_bf16(xn[0], xn[1]); xs.w = cvt_pk_bf16(xn[2], xn[3]); }
;                 }
;                 *(u32x4*)(x + EPIRES_OFF(g, bj)) = xs;
;             }
	v_and_b32_e32 v159, 0xffff0000, v159
	v_fma_f32 v118, v118, v94, v128
	v_fma_f32 v119, v119, v95, v159
	v_mul_f32_e32 v158, v117, v117
	v_mul_f32_e32 v159, v119, v119
	v_fmac_f32_e32 v158, v116, v116
	v_fmac_f32_e32 v159, v118, v118
	v_add_f32_e32 v158, v158, v159
	v_lshlrev_b32_e32 v128, 16, v160
	v_and_b32_e32 v160, 0xffff0000, v160
	v_fma_f32 v112, v112, v88, v128
	v_fma_f32 v113, v113, v89, v160
	v_lshlrev_b32_e32 v128, 16, v161
	v_and_b32_e32 v161, 0xffff0000, v161
	v_fma_f32 v114, v114, v90, v128
	v_fma_f32 v115, v115, v91, v161
	v_mul_f32_e32 v160, v113, v113
	v_mul_f32_e32 v161, v115, v115
	v_fmac_f32_e32 v160, v112, v112
	v_fmac_f32_e32 v161, v114, v114
	v_add_f32_e32 v160, v160, v161
	v_add_f32_e32 v128, v124, v158
	v_add_f32_e32 v128, v128, v160
	v_cvt_pk_bf16_f32 v158, v116, v117
	v_cvt_pk_bf16_f32 v159, v118, v119
	v_cvt_pk_bf16_f32 v160, v112, v113
	v_cvt_pk_bf16_f32 v161, v114, v115
	v_mov_b32_e32 v124, v128
	global_store_dwordx4 v[190:191], v[158:161], off offset:-2048
	v_lshlrev_b32_e32 v128, 16, v162
	v_and_b32_e32 v162, 0xffff0000, v162
	v_fma_f32 v104, v104, v108, v128
	v_fma_f32 v105, v105, v109, v162
	v_lshlrev_b32_e32 v128, 16, v163
	v_and_b32_e32 v163, 0xffff0000, v163
	v_fma_f32 v106, v106, v110, v128
	v_fma_f32 v107, v107, v111, v163
	v_mul_f32_e32 v162, v105, v105
	v_mul_f32_e32 v163, v107, v107
	v_fmac_f32_e32 v162, v104, v104
	v_fmac_f32_e32 v163, v106, v106
	v_add_f32_e32 v162, v162, v163
	v_lshlrev_b32_e32 v128, 16, v164
	v_and_b32_e32 v164, 0xffff0000, v164
	v_fma_f32 v96, v96, v100, v128
	v_fma_f32 v97, v97, v101, v164
	v_lshlrev_b32_e32 v128, 16, v165
	v_and_b32_e32 v165, 0xffff0000, v165
	v_fma_f32 v98, v98, v102, v128
	v_fma_f32 v99, v99, v103, v165
	v_mul_f32_e32 v164, v97, v97
	v_mul_f32_e32 v165, v99, v99
	v_fmac_f32_e32 v164, v96, v96
	v_fmac_f32_e32 v165, v98, v98
	v_add_f32_e32 v164, v164, v165
	v_add_f32_e32 v128, v162, v164
	v_cvt_pk_bf16_f32 v162, v104, v105
	v_cvt_pk_bf16_f32 v163, v106, v107
	v_cvt_pk_bf16_f32 v164, v96, v97
	v_cvt_pk_bf16_f32 v165, v98, v99
	v_mov_b32_e32 v104, v128
	global_store_dwordx4 v[172:173], v[162:165], off
	v_lshlrev_b32_e32 v128, 16, v166
	v_and_b32_e32 v166, 0xffff0000, v166
	v_fma_f32 v84, v84, v92, v128
	v_fma_f32 v85, v85, v93, v166
	v_lshlrev_b32_e32 v128, 16, v167
	v_and_b32_e32 v167, 0xffff0000, v167
	v_fma_f32 v86, v86, v94, v128
	v_fma_f32 v87, v87, v95, v167
	v_mul_f32_e32 v166, v85, v85
	v_mul_f32_e32 v167, v87, v87
	v_fmac_f32_e32 v166, v84, v84
	v_fmac_f32_e32 v167, v86, v86
	v_add_f32_e32 v166, v166, v167
	v_lshlrev_b32_e32 v128, 16, v168
	v_and_b32_e32 v168, 0xffff0000, v168
	v_fma_f32 v80, v80, v88, v128
	v_fma_f32 v81, v81, v89, v168
	v_lshlrev_b32_e32 v128, 16, v169
	v_and_b32_e32 v169, 0xffff0000, v169
	v_fma_f32 v82, v82, v90, v128
	v_fma_f32 v83, v83, v91, v169
	v_mul_f32_e32 v168, v81, v81
	v_mul_f32_e32 v169, v83, v83
	v_fmac_f32_e32 v168, v80, v80
	v_fmac_f32_e32 v169, v82, v82
	v_add_f32_e32 v168, v168, v169
	v_add_f32_e32 v128, v104, v166
	v_add_f32_e32 v128, v128, v168
	v_cvt_pk_bf16_f32 v166, v84, v85
	v_cvt_pk_bf16_f32 v167, v86, v87
	v_cvt_pk_bf16_f32 v168, v80, v81
	v_cvt_pk_bf16_f32 v169, v82, v83
	v_mov_b32_e32 v104, v128
	global_store_dwordx4 v[190:191], v[166:169], off
	v_lshlrev_b32_e32 v128, 16, v196
	v_and_b32_e32 v196, 0xffff0000, v196
	v_fma_f32 v76, v76, v108, v128
	v_fma_f32 v77, v77, v109, v196
	v_lshlrev_b32_e32 v128, 16, v197
	v_and_b32_e32 v197, 0xffff0000, v197
	v_fma_f32 v78, v78, v110, v128
	v_fma_f32 v79, v79, v111, v197
	v_mul_f32_e32 v196, v77, v77
	v_mul_f32_e32 v197, v79, v79
	v_fmac_f32_e32 v196, v76, v76
	v_fmac_f32_e32 v197, v78, v78
	v_add_f32_e32 v196, v196, v197
	v_lshlrev_b32_e32 v128, 16, v198
	v_and_b32_e32 v198, 0xffff0000, v198
	v_fma_f32 v72, v72, v100, v128
	v_fma_f32 v73, v73, v101, v198
	v_lshlrev_b32_e32 v128, 16, v199
	v_and_b32_e32 v199, 0xffff0000, v199
	v_fma_f32 v74, v74, v102, v128
	v_fma_f32 v75, v75, v103, v199
	v_mul_f32_e32 v198, v73, v73
	v_mul_f32_e32 v199, v75, v75
	v_fmac_f32_e32 v198, v72, v72
	v_fmac_f32_e32 v199, v74, v74
	v_add_f32_e32 v198, v198, v199
	v_add_f32_e32 v128, v196, v198
	v_cvt_pk_bf16_f32 v196, v76, v77
	v_cvt_pk_bf16_f32 v197, v78, v79
	v_cvt_pk_bf16_f32 v198, v72, v73
	v_cvt_pk_bf16_f32 v199, v74, v75
	v_mov_b32_e32 v76, v128
	global_store_dwordx4 v[172:173], v[196:199], off offset:2048
	v_lshlrev_b32_e32 v128, 16, v200
	v_and_b32_e32 v200, 0xffff0000, v200
	v_fma_f32 v68, v68, v92, v128
	v_fma_f32 v69, v69, v93, v200
	v_lshlrev_b32_e32 v128, 16, v201
	v_and_b32_e32 v201, 0xffff0000, v201
	v_fma_f32 v70, v70, v94, v128
	v_fma_f32 v71, v71, v95, v201
	v_mul_f32_e32 v200, v69, v69
	v_mul_f32_e32 v201, v71, v71
	v_fmac_f32_e32 v200, v68, v68
	v_fmac_f32_e32 v201, v70, v70
	v_add_f32_e32 v200, v200, v201
	v_lshlrev_b32_e32 v128, 16, v202
	v_and_b32_e32 v202, 0xffff0000, v202
	v_fma_f32 v64, v64, v88, v128
	v_fma_f32 v65, v65, v89, v202
	v_lshlrev_b32_e32 v128, 16, v203
	v_and_b32_e32 v203, 0xffff0000, v203
	v_fma_f32 v66, v66, v90, v128
	v_fma_f32 v67, v67, v91, v203
	v_mul_f32_e32 v202, v65, v65
	v_mul_f32_e32 v203, v67, v67
	v_fmac_f32_e32 v202, v64, v64
	v_fmac_f32_e32 v203, v66, v66
	v_add_f32_e32 v202, v202, v203
	v_add_f32_e32 v128, v76, v200
	v_add_f32_e32 v128, v128, v202
	v_cvt_pk_bf16_f32 v200, v68, v69
	v_cvt_pk_bf16_f32 v201, v70, v71
	v_cvt_pk_bf16_f32 v202, v64, v65
	v_cvt_pk_bf16_f32 v203, v66, v67
	v_mov_b32_e32 v76, v128
	global_store_dwordx4 v[190:191], v[200:203], off offset:2048
	v_lshlrev_b32_e32 v128, 16, v204
	v_and_b32_e32 v204, 0xffff0000, v204
	v_fma_f32 v60, v60, v108, v128
	v_fma_f32 v61, v61, v109, v204
	v_lshlrev_b32_e32 v128, 16, v205
; __device__ __forceinline__ unsigned cvt_pk_bf16(float lo, float hi) { const f32x2_t v = {lo, hi}; const bf16x2_t b = __builtin_convertvector(v, bf16x2_t); return __builtin_bit_cast(unsigned, b); }
;     __device__ __forceinline__ void operator()(const f32x4 (&acc)[2][2][4][2], const Unit& u, int wr, int wc, int fr, int fq, int ui) const {
;     ...
;             for (int bj = 0; bj < 2; ++bj) {
;                 u32x4 xs;
; #pragma unroll
;                 for (int n = 0; n < 2; ++n) {
;                     const unsigned p0 = xb[g % 3][bj][2 * n], p1 = xb[g % 3][bj][2 * n + 1];
;                     const f32x4 xo = {__builtin_bit_cast(float, p0 << 16), __builtin_bit_cast(float, p0 & 0xFFFF0000u), __builtin_bit_cast(float, p1 << 16), __builtin_bit_cast(float, p1 & 0xFFFF0000u)};
;                     const f32x4 xn = xo + cr[bj][n] * acc[ai][bj][m][n];
;                     sq += (xn[0] * xn[0] + xn[1] * xn[1]) + (xn[2] * xn[2] + xn[3] * xn[3]);
;                     if (n == 0) { xs.x = cvt_pk_bf16(xn[0], xn[1]); xs.y = cvt_pk_bf16(xn[2], xn[3]); } else { xs.z = cvt_pk_bf16(xn[0], xn[1]); xs.w = cvt_pk_bf16(xn[2], xn[3]); }
;                 }
;                 *(u32x4*)(x + EPIRES_OFF(g, bj)) = xs;
;             }
	v_and_b32_e32 v205, 0xffff0000, v205
	v_fma_f32 v62, v62, v110, v128
	v_fma_f32 v63, v63, v111, v205
	v_mul_f32_e32 v204, v61, v61
	v_mul_f32_e32 v205, v63, v63
	v_fmac_f32_e32 v204, v60, v60
	v_fmac_f32_e32 v205, v62, v62
	v_add_f32_e32 v204, v204, v205
	v_lshlrev_b32_e32 v128, 16, v206
	v_and_b32_e32 v206, 0xffff0000, v206
	v_fma_f32 v56, v56, v100, v128
	v_fma_f32 v57, v57, v101, v206
	v_lshlrev_b32_e32 v128, 16, v207
	v_and_b32_e32 v207, 0xffff0000, v207
	v_fma_f32 v58, v58, v102, v128
	v_fma_f32 v59, v59, v103, v207
	v_mul_f32_e32 v206, v57, v57
	v_mul_f32_e32 v207, v59, v59
	v_fmac_f32_e32 v206, v56, v56
	v_fmac_f32_e32 v207, v58, v58
	v_add_f32_e32 v206, v206, v207
	v_add_f32_e32 v128, v204, v206
	v_cvt_pk_bf16_f32 v204, v60, v61
	v_cvt_pk_bf16_f32 v205, v62, v63
	v_cvt_pk_bf16_f32 v206, v56, v57
	v_cvt_pk_bf16_f32 v207, v58, v59
	v_mov_b32_e32 v60, v128
	global_store_dwordx4 v[174:175], v[204:207], off offset:-4096
	v_lshlrev_b32_e32 v128, 16, v208
	v_and_b32_e32 v208, 0xffff0000, v208
	v_fma_f32 v52, v52, v92, v128
	v_fma_f32 v53, v53, v93, v208
	v_lshlrev_b32_e32 v128, 16, v209
	v_and_b32_e32 v209, 0xffff0000, v209
	v_fma_f32 v54, v54, v94, v128
	v_fma_f32 v55, v55, v95, v209
	v_mul_f32_e32 v208, v53, v53
	v_mul_f32_e32 v209, v55, v55
	v_fmac_f32_e32 v208, v52, v52
	v_fmac_f32_e32 v209, v54, v54
	v_add_f32_e32 v208, v208, v209
	v_lshlrev_b32_e32 v128, 16, v210
	v_and_b32_e32 v210, 0xffff0000, v210
	v_fma_f32 v48, v48, v88, v128
	v_fma_f32 v49, v49, v89, v210
	v_lshlrev_b32_e32 v128, 16, v211
	v_and_b32_e32 v211, 0xffff0000, v211
	v_fma_f32 v50, v50, v90, v128
	v_fma_f32 v51, v51, v91, v211
	v_mul_f32_e32 v210, v49, v49
	v_mul_f32_e32 v211, v51, v51
	v_fmac_f32_e32 v210, v48, v48
	v_fmac_f32_e32 v211, v50, v50
	v_add_f32_e32 v210, v210, v211
	v_add_f32_e32 v128, v60, v208
	v_add_f32_e32 v128, v128, v210
	v_cvt_pk_bf16_f32 v208, v52, v53
	v_cvt_pk_bf16_f32 v209, v54, v55
	v_cvt_pk_bf16_f32 v210, v48, v49
	v_cvt_pk_bf16_f32 v211, v50, v51
	v_mov_b32_e32 v60, v128
	global_store_dwordx4 v[192:193], v[208:211], off offset:-4096
	v_lshlrev_b32_e32 v128, 16, v212
	v_and_b32_e32 v212, 0xffff0000, v212
	v_fma_f32 v44, v44, v108, v128
	v_fma_f32 v45, v45, v109, v212
	v_lshlrev_b32_e32 v128, 16, v213
	v_and_b32_e32 v213, 0xffff0000, v213
	v_fma_f32 v46, v46, v110, v128
	v_fma_f32 v47, v47, v111, v213
	v_mul_f32_e32 v212, v45, v45
	v_mul_f32_e32 v213, v47, v47
	v_fmac_f32_e32 v212, v44, v44
	v_fmac_f32_e32 v213, v46, v46
	v_add_f32_e32 v212, v212, v213
	v_lshlrev_b32_e32 v128, 16, v214
	v_and_b32_e32 v214, 0xffff0000, v214
	v_fma_f32 v40, v40, v100, v128
	v_fma_f32 v41, v41, v101, v214
	v_lshlrev_b32_e32 v128, 16, v215
	v_and_b32_e32 v215, 0xffff0000, v215
	v_fma_f32 v42, v42, v102, v128
	v_fma_f32 v43, v43, v103, v215
	v_mul_f32_e32 v214, v41, v41
	v_mul_f32_e32 v215, v43, v43
	v_fmac_f32_e32 v214, v40, v40
	v_fmac_f32_e32 v215, v42, v42
	v_add_f32_e32 v214, v214, v215
	v_add_f32_e32 v128, v212, v214
	v_cvt_pk_bf16_f32 v212, v44, v45
	v_cvt_pk_bf16_f32 v213, v46, v47
	v_cvt_pk_bf16_f32 v214, v40, v41
	v_cvt_pk_bf16_f32 v215, v42, v43
	v_mov_b32_e32 v44, v128
	global_store_dwordx4 v[174:175], v[212:215], off offset:-2048
	v_lshlrev_b32_e32 v128, 16, v216
	v_and_b32_e32 v216, 0xffff0000, v216
	v_fma_f32 v36, v36, v92, v128
	v_fma_f32 v37, v37, v93, v216
	v_lshlrev_b32_e32 v128, 16, v217
	v_and_b32_e32 v217, 0xffff0000, v217
	v_fma_f32 v38, v38, v94, v128
	v_fma_f32 v39, v39, v95, v217
	v_mul_f32_e32 v216, v37, v37
	v_mul_f32_e32 v217, v39, v39
	v_fmac_f32_e32 v216, v36, v36
	v_fmac_f32_e32 v217, v38, v38
	v_add_f32_e32 v216, v216, v217
	v_lshlrev_b32_e32 v128, 16, v218
	v_and_b32_e32 v218, 0xffff0000, v218
	v_fma_f32 v32, v32, v88, v128
	v_fma_f32 v33, v33, v89, v218
	v_lshlrev_b32_e32 v128, 16, v219
	v_and_b32_e32 v219, 0xffff0000, v219
	v_fma_f32 v34, v34, v90, v128
	v_fma_f32 v35, v35, v91, v219
	v_mul_f32_e32 v218, v33, v33
	v_mul_f32_e32 v219, v35, v35
	v_fmac_f32_e32 v218, v32, v32
	v_fmac_f32_e32 v219, v34, v34
	v_add_f32_e32 v218, v218, v219
	v_add_f32_e32 v128, v44, v216
	v_add_f32_e32 v128, v128, v218
	v_cvt_pk_bf16_f32 v216, v36, v37
	v_cvt_pk_bf16_f32 v217, v38, v39
	v_cvt_pk_bf16_f32 v218, v32, v33
	v_cvt_pk_bf16_f32 v219, v34, v35
	v_mov_b32_e32 v44, v128
	global_store_dwordx4 v[192:193], v[216:219], off offset:-2048
	v_lshlrev_b32_e32 v128, 16, v220
	v_and_b32_e32 v220, 0xffff0000, v220
	v_fma_f32 v28, v28, v108, v128
	v_fma_f32 v29, v29, v109, v220
	v_lshlrev_b32_e32 v128, 16, v221
	v_and_b32_e32 v221, 0xffff0000, v221
	v_fma_f32 v30, v30, v110, v128
	v_fma_f32 v31, v31, v111, v221
	v_mul_f32_e32 v220, v29, v29
	v_mul_f32_e32 v221, v31, v31
	v_fmac_f32_e32 v220, v28, v28
	v_fmac_f32_e32 v221, v30, v30
	v_add_f32_e32 v220, v220, v221
	v_lshlrev_b32_e32 v128, 16, v222
	v_and_b32_e32 v222, 0xffff0000, v222
	v_fma_f32 v24, v24, v100, v128
	v_fma_f32 v25, v25, v101, v222
	v_lshlrev_b32_e32 v128, 16, v223
	v_and_b32_e32 v223, 0xffff0000, v223
	v_fma_f32 v26, v26, v102, v128
	v_fma_f32 v27, v27, v103, v223
	v_mul_f32_e32 v222, v25, v25
	v_mul_f32_e32 v223, v27, v27
	v_fmac_f32_e32 v222, v24, v24
	v_fmac_f32_e32 v223, v26, v26
	v_add_f32_e32 v222, v222, v223
	v_add_f32_e32 v128, v220, v222
	v_cvt_pk_bf16_f32 v220, v28, v29
	v_cvt_pk_bf16_f32 v221, v30, v31
	v_cvt_pk_bf16_f32 v222, v24, v25
	v_cvt_pk_bf16_f32 v223, v26, v27
	v_mov_b32_e32 v28, v128
	global_store_dwordx4 v[174:175], v[220:223], off
	v_lshlrev_b32_e32 v128, 16, v224
	v_and_b32_e32 v224, 0xffff0000, v224
	v_fma_f32 v20, v20, v92, v128
	v_fma_f32 v21, v21, v93, v224
	v_lshlrev_b32_e32 v128, 16, v225
	v_and_b32_e32 v225, 0xffff0000, v225
	v_fma_f32 v22, v22, v94, v128
	v_fma_f32 v23, v23, v95, v225
	v_mul_f32_e32 v224, v21, v21
	v_mul_f32_e32 v225, v23, v23
	v_fmac_f32_e32 v224, v20, v20
	v_fmac_f32_e32 v225, v22, v22
	v_add_f32_e32 v224, v224, v225
	v_lshlrev_b32_e32 v128, 16, v226
	v_and_b32_e32 v226, 0xffff0000, v226
	v_fma_f32 v16, v16, v88, v128
	v_fma_f32 v17, v17, v89, v226
	v_lshlrev_b32_e32 v128, 16, v227
	v_and_b32_e32 v227, 0xffff0000, v227
	v_fma_f32 v18, v18, v90, v128
	v_fma_f32 v19, v19, v91, v227
	v_mul_f32_e32 v226, v17, v17
	v_mul_f32_e32 v227, v19, v19
	v_fmac_f32_e32 v226, v16, v16
	v_fmac_f32_e32 v227, v18, v18
	v_add_f32_e32 v226, v226, v227
	v_add_f32_e32 v128, v28, v224
	v_add_f32_e32 v128, v128, v226
	v_cvt_pk_bf16_f32 v224, v20, v21
	v_cvt_pk_bf16_f32 v225, v22, v23
	v_cvt_pk_bf16_f32 v226, v16, v17
	v_cvt_pk_bf16_f32 v227, v18, v19
	v_mov_b32_e32 v28, v128
	global_store_dwordx4 v[192:193], v[224:227], off
	s_waitcnt vmcnt(12)
; __device__ __forceinline__ unsigned cvt_pk_bf16(float lo, float hi) { const f32x2_t v = {lo, hi}; const bf16x2_t b = __builtin_convertvector(v, bf16x2_t); return __builtin_bit_cast(unsigned, b); }
;     __device__ __forceinline__ void operator()(const f32x4 (&acc)[2][2][4][2], const Unit& u, int wr, int wc, int fr, int fq, int ui) const {
;     ...
;             for (int bj = 0; bj < 2; ++bj) {
;                 u32x4 xs;
; #pragma unroll
;                 for (int n = 0; n < 2; ++n) {
;                     const unsigned p0 = xb[g % 3][bj][2 * n], p1 = xb[g % 3][bj][2 * n + 1];
;                     const f32x4 xo = {__builtin_bit_cast(float, p0 << 16), __builtin_bit_cast(float, p0 & 0xFFFF0000u), __builtin_bit_cast(float, p1 << 16), __builtin_bit_cast(float, p1 & 0xFFFF0000u)};
;                     const f32x4 xn = xo + cr[bj][n] * acc[ai][bj][m][n];
;                     sq += (xn[0] * xn[0] + xn[1] * xn[1]) + (xn[2] * xn[2] + xn[3] * xn[3]);
;                     if (n == 0) { xs.x = cvt_pk_bf16(xn[0], xn[1]); xs.y = cvt_pk_bf16(xn[2], xn[3]); } else { xs.z = cvt_pk_bf16(xn[0], xn[1]); xs.w = cvt_pk_bf16(xn[2], xn[3]); }
;                 }
;                 *(u32x4*)(x + EPIRES_OFF(g, bj)) = xs;
;             }
;             sq += __shfl_xor(sq, 16); sq += __shfl_xor(sq, 32);
;             if (fq == 0) ss[(size_t)row_ * 32 + u.pn * 4 + wc] = sq;
	v_lshlrev_b32_e32 v128, 16, v138
	v_and_b32_e32 v138, 0xffff0000, v138
	v_fma_f32 v12, v12, v108, v128
	v_fma_f32 v13, v13, v109, v138
	v_lshlrev_b32_e32 v128, 16, v139
	v_and_b32_e32 v139, 0xffff0000, v139
	v_fma_f32 v14, v14, v110, v128
	v_fma_f32 v15, v15, v111, v139
	v_mul_f32_e32 v138, v13, v13
	v_mul_f32_e32 v139, v15, v15
	v_fmac_f32_e32 v138, v12, v12
	v_fmac_f32_e32 v139, v14, v14
	v_add_f32_e32 v138, v138, v139
	v_lshlrev_b32_e32 v128, 16, v140
	v_and_b32_e32 v140, 0xffff0000, v140
	v_fma_f32 v8, v8, v100, v128
	v_fma_f32 v9, v9, v101, v140
	v_lshlrev_b32_e32 v128, 16, v141
	v_and_b32_e32 v141, 0xffff0000, v141
	v_fma_f32 v10, v10, v102, v128
	v_fma_f32 v11, v11, v103, v141
	v_mul_f32_e32 v140, v9, v9
	v_mul_f32_e32 v141, v11, v11
	v_fmac_f32_e32 v140, v8, v8
	v_fmac_f32_e32 v141, v10, v10
	v_add_f32_e32 v140, v140, v141
	v_add_f32_e32 v128, v138, v140
	v_cvt_pk_bf16_f32 v138, v12, v13
	v_cvt_pk_bf16_f32 v139, v14, v15
	v_cvt_pk_bf16_f32 v140, v8, v9
	v_cvt_pk_bf16_f32 v141, v10, v11
	v_mov_b32_e32 v12, v128
	global_store_dwordx4 v[174:175], v[138:141], off offset:2048
	v_lshlrev_b32_e32 v128, 16, v134
	v_and_b32_e32 v134, 0xffff0000, v134
	v_fma_f32 v4, v4, v92, v128
	v_fma_f32 v5, v5, v93, v134
	v_lshlrev_b32_e32 v128, 16, v135
	v_and_b32_e32 v135, 0xffff0000, v135
	v_fma_f32 v6, v6, v94, v128
	v_fma_f32 v7, v7, v95, v135
	v_mul_f32_e32 v134, v5, v5
	v_mul_f32_e32 v135, v7, v7
	v_fmac_f32_e32 v134, v4, v4
	v_fmac_f32_e32 v135, v6, v6
	v_add_f32_e32 v134, v134, v135
	v_lshlrev_b32_e32 v128, 16, v136
	v_and_b32_e32 v136, 0xffff0000, v136
	v_fma_f32 v0, v0, v88, v128
	v_fma_f32 v1, v1, v89, v136
	v_lshlrev_b32_e32 v128, 16, v137
	v_and_b32_e32 v137, 0xffff0000, v137
	v_fma_f32 v2, v2, v90, v128
	v_fma_f32 v3, v3, v91, v137
	v_mul_f32_e32 v136, v1, v1
	v_mul_f32_e32 v137, v3, v3
	v_fmac_f32_e32 v136, v0, v0
	v_fmac_f32_e32 v137, v2, v2
	v_add_f32_e32 v136, v136, v137
	v_add_f32_e32 v128, v12, v134
	v_add_f32_e32 v128, v128, v136
	v_cvt_pk_bf16_f32 v134, v4, v5
	v_cvt_pk_bf16_f32 v135, v6, v7
	v_cvt_pk_bf16_f32 v136, v0, v1
	v_cvt_pk_bf16_f32 v137, v2, v3
	v_mov_b32_e32 v12, v128
	global_store_dwordx4 v[192:193], v[134:137], off offset:2048
	v_xor_b32_e32 v128, 16, v228
	v_add_u32_e32 v172, 64, v171
	v_xor_b32_e32 v173, 32, v228
	v_cmp_lt_i32_e32 vcc, v128, v172
	s_nop 1
	v_cndmask_b32_e32 v128, v228, v128, vcc
	v_cmp_lt_i32_e32 vcc, v173, v172
	v_lshlrev_b32_e32 v128, 2, v128
	v_cndmask_b32_e32 v172, v228, v173, vcc
	v_lshlrev_b32_e32 v196, 2, v172
	v_lshl_add_u32 v190, s49, 8, v184
	s_lshl_b32 s18, s48, 2
	s_ashr_i32 s19, s18, 31
	ds_bpermute_b32 v146, v128, v142
	ds_bpermute_b32 v147, v128, v124
	ds_bpermute_b32 v148, v128, v104
	ds_bpermute_b32 v149, v128, v76
	ds_bpermute_b32 v150, v128, v60
	ds_bpermute_b32 v151, v128, v44
	ds_bpermute_b32 v152, v128, v28
	ds_bpermute_b32 v153, v128, v12
	s_waitcnt lgkmcnt(0)
	v_add_f32_e32 v142, v142, v146
	v_add_f32_e32 v124, v124, v147
	v_add_f32_e32 v104, v104, v148
	v_add_f32_e32 v76, v76, v149
	v_add_f32_e32 v60, v60, v150
	v_add_f32_e32 v44, v44, v151
	v_add_f32_e32 v28, v28, v152
	v_add_f32_e32 v12, v12, v153
	ds_bpermute_b32 v146, v196, v142
	ds_bpermute_b32 v147, v196, v124
	ds_bpermute_b32 v148, v196, v104
	ds_bpermute_b32 v149, v196, v76
	ds_bpermute_b32 v150, v196, v60
	ds_bpermute_b32 v151, v196, v44
	ds_bpermute_b32 v152, v196, v28
	ds_bpermute_b32 v153, v196, v12
	s_and_saveexec_b64 s[20:21], s[4:5]
	s_waitcnt lgkmcnt(0)
	s_lshl_b32 s64, s36, 2
	v_add_f32_e32 v142, v142, v146
	v_or_b32_e32 v154, 0, v190
	v_ashrrev_i32_e32 v155, 31, v154
	v_lshlrev_b64 v[154:155], 7, v[154:155]
	v_lshl_add_u64 v[154:155], s[12:13], 0, v[154:155]
	v_lshl_add_u64 v[154:155], s[18:19], 2, v[154:155]
	v_lshl_add_u64 v[154:155], v[154:155], 0, s[64:65]
	global_store_dword v[154:155], v142, off
	v_add_f32_e32 v124, v124, v147
	v_or_b32_e32 v154, 16, v190
	v_ashrrev_i32_e32 v155, 31, v154
	v_lshlrev_b64 v[154:155], 7, v[154:155]
	v_lshl_add_u64 v[154:155], s[12:13], 0, v[154:155]
	v_lshl_add_u64 v[154:155], s[18:19], 2, v[154:155]
	v_lshl_add_u64 v[154:155], v[154:155], 0, s[64:65]
	global_store_dword v[154:155], v124, off
	v_add_f32_e32 v104, v104, v148
	v_or_b32_e32 v154, 32, v190
	v_ashrrev_i32_e32 v155, 31, v154
	v_lshlrev_b64 v[154:155], 7, v[154:155]
	v_lshl_add_u64 v[154:155], s[12:13], 0, v[154:155]
	v_lshl_add_u64 v[154:155], s[18:19], 2, v[154:155]
	v_lshl_add_u64 v[154:155], v[154:155], 0, s[64:65]
	global_store_dword v[154:155], v104, off
	v_add_f32_e32 v76, v76, v149
	v_or_b32_e32 v154, 48, v190
	v_ashrrev_i32_e32 v155, 31, v154
	v_lshlrev_b64 v[154:155], 7, v[154:155]
	v_lshl_add_u64 v[154:155], s[12:13], 0, v[154:155]
	v_lshl_add_u64 v[154:155], s[18:19], 2, v[154:155]
	v_lshl_add_u64 v[154:155], v[154:155], 0, s[64:65]
	global_store_dword v[154:155], v76, off
	v_add_f32_e32 v60, v60, v150
	v_or_b32_e32 v154, 128, v190
	v_ashrrev_i32_e32 v155, 31, v154
	v_lshlrev_b64 v[154:155], 7, v[154:155]
	v_lshl_add_u64 v[154:155], s[12:13], 0, v[154:155]
	v_lshl_add_u64 v[154:155], s[18:19], 2, v[154:155]
	v_lshl_add_u64 v[154:155], v[154:155], 0, s[64:65]
	global_store_dword v[154:155], v60, off
	v_add_f32_e32 v44, v44, v151
	v_or_b32_e32 v154, 144, v190
	v_ashrrev_i32_e32 v155, 31, v154
	v_lshlrev_b64 v[154:155], 7, v[154:155]
	v_lshl_add_u64 v[154:155], s[12:13], 0, v[154:155]
	v_lshl_add_u64 v[154:155], s[18:19], 2, v[154:155]
	v_lshl_add_u64 v[154:155], v[154:155], 0, s[64:65]
	global_store_dword v[154:155], v44, off
	v_add_f32_e32 v28, v28, v152
	v_or_b32_e32 v154, 160, v190
	v_ashrrev_i32_e32 v155, 31, v154
	v_lshlrev_b64 v[154:155], 7, v[154:155]
	v_lshl_add_u64 v[154:155], s[12:13], 0, v[154:155]
	v_lshl_add_u64 v[154:155], s[18:19], 2, v[154:155]
	v_lshl_add_u64 v[154:155], v[154:155], 0, s[64:65]
	global_store_dword v[154:155], v28, off
	v_add_f32_e32 v12, v12, v153
	v_or_b32_e32 v154, 176, v190
	v_ashrrev_i32_e32 v155, 31, v154
	v_lshlrev_b64 v[154:155], 7, v[154:155]
	v_lshl_add_u64 v[154:155], s[12:13], 0, v[154:155]
	v_lshl_add_u64 v[154:155], s[18:19], 2, v[154:155]
	v_lshl_add_u64 v[154:155], v[154:155], 0, s[64:65]
	global_store_dword v[154:155], v12, off
